# attention epilogue: sub-LN gain vectors loaded up front (16 serialized L2 round trips removed); shared-down epilogue: 16 x1s read-modify-writes pipelined
# speedup vs baseline: 1.0644x; 1.0097x over previous
.LBB0_324:
	ds_bpermute_b32 v2, v1, v214
	ds_bpermute_b32 v4, v1, v215
	v_mov_b32_e32 v5, s49
	ds_read_b32 v5, v5
	v_ashrrev_i32_e32 v197, 31, v196
	s_waitcnt lgkmcnt(2)
	v_add_f32_e32 v2, v214, v2
	v_div_scale_f32 v6, s[6:7], v2, v2, 1.0
	v_rcp_f32_e32 v7, v6
	v_div_scale_f32 v8, vcc, 1.0, v2, 1.0
	s_waitcnt lgkmcnt(1)
	v_add_f32_e32 v4, v215, v4
	v_fma_f32 v9, -v6, v7, 1.0
	v_fmac_f32_e32 v7, v9, v7
	v_mul_f32_e32 v9, v8, v7
	v_fma_f32 v10, -v6, v9, v8
	v_fmac_f32_e32 v9, v10, v7
	v_fma_f32 v6, -v6, v9, v8
	s_waitcnt lgkmcnt(0)
	v_div_scale_f32 v8, s[6:7], v4, v4, v5
	v_rcp_f32_e32 v10, v8
	v_div_fmas_f32 v6, v6, v7, v9
	v_div_fixup_f32 v2, v6, v2, 1.0
	s_load_dwordx2 s[6:7], s[34:35], 0x58
	v_fma_f32 v6, -v8, v10, 1.0
	v_fmac_f32_e32 v10, v6, v10
	v_div_scale_f32 v6, vcc, v5, v4, v5
	v_mul_f32_e32 v7, v6, v10
	v_fma_f32 v9, -v8, v7, v6
	v_fmac_f32_e32 v7, v9, v10
	v_fma_f32 v6, -v8, v7, v6
	v_div_fmas_f32 v6, v6, v10, v7
	v_div_fixup_f32 v10, v6, v4, v5
	v_mul_f32_e32 v4, v130, v10
	v_fma_f32 v12, v114, v2, -v4
	v_mul_f32_e32 v4, v131, v10
	v_fma_f32 v13, v115, v2, -v4
	v_mul_f32_e32 v4, v132, v10
	v_fma_f32 v14, v116, v2, -v4
	v_mul_f32_e32 v4, v133, v10
	v_fma_f32 v15, v117, v2, -v4
	v_mul_f32_e32 v4, v134, v10
	v_fma_f32 v16, v118, v2, -v4
	v_mul_f32_e32 v4, v135, v10
	v_fma_f32 v17, v119, v2, -v4
	v_mul_f32_e32 v4, v136, v10
	v_fma_f32 v114, v120, v2, -v4
	v_mul_f32_e32 v4, v137, v10
	v_fma_f32 v115, v121, v2, -v4
	v_mul_f32_e32 v4, v138, v10
	v_fma_f32 v116, v122, v2, -v4
	v_mul_f32_e32 v4, v139, v10
	v_fma_f32 v117, v123, v2, -v4
	v_mul_f32_e32 v4, v140, v10
	v_fma_f32 v118, v124, v2, -v4
	v_mul_f32_e32 v4, v141, v10
	v_fma_f32 v119, v125, v2, -v4
	v_mul_f32_e32 v4, v142, v10
	v_fma_f32 v120, v126, v2, -v4
	v_mul_f32_e32 v4, v143, v10
	v_fma_f32 v121, v127, v2, -v4
	v_mul_f32_e32 v4, v144, v10
	v_fma_f32 v122, v128, v2, -v4
	v_mul_f32_e32 v4, v145, v10
	v_fma_f32 v123, v129, v2, -v4
	v_mul_f32_e32 v4, v98, v10
	v_fma_f32 v82, v82, v2, -v4
	v_mul_f32_e32 v4, v99, v10
	v_fma_f32 v83, v83, v2, -v4
	v_mul_f32_e32 v4, v100, v10
	v_fma_f32 v84, v84, v2, -v4
	v_mul_f32_e32 v4, v101, v10
	v_fma_f32 v85, v85, v2, -v4
	v_mul_f32_e32 v4, v102, v10
	v_fma_f32 v86, v86, v2, -v4
	v_mul_f32_e32 v4, v103, v10
	v_fma_f32 v87, v87, v2, -v4
	v_mul_f32_e32 v4, v104, v10
	v_fma_f32 v88, v88, v2, -v4
	v_mul_f32_e32 v4, v105, v10
	v_fma_f32 v89, v89, v2, -v4
	v_mul_f32_e32 v4, v106, v10
	v_fma_f32 v90, v90, v2, -v4
	v_mul_f32_e32 v4, v107, v10
	v_fma_f32 v91, v91, v2, -v4
	v_mul_f32_e32 v4, v108, v10
	v_fma_f32 v92, v92, v2, -v4
	v_mul_f32_e32 v4, v109, v10
	v_fma_f32 v93, v93, v2, -v4
	v_mul_f32_e32 v4, v110, v10
	v_fma_f32 v94, v94, v2, -v4
	v_mul_f32_e32 v4, v111, v10
	v_fma_f32 v95, v95, v2, -v4
	v_mul_f32_e32 v4, v112, v10
	v_fma_f32 v96, v96, v2, -v4
	v_mul_f32_e32 v4, v113, v10
	v_fma_f32 v97, v97, v2, -v4
	v_mul_f32_e32 v4, v66, v10
	v_mul_f32_e32 v11, v13, v13
	v_fma_f32 v50, v50, v2, -v4
	v_mul_f32_e32 v4, v67, v10
	v_fmac_f32_e32 v11, v12, v12
	v_fma_f32 v51, v51, v2, -v4
	v_mul_f32_e32 v4, v68, v10
	v_fmac_f32_e32 v11, v14, v14
	v_fma_f32 v52, v52, v2, -v4
	v_mul_f32_e32 v4, v69, v10
	v_fmac_f32_e32 v11, v15, v15
	v_fma_f32 v53, v53, v2, -v4
	v_mul_f32_e32 v4, v70, v10
	v_fmac_f32_e32 v11, v16, v16
	v_fma_f32 v54, v54, v2, -v4
	v_mul_f32_e32 v4, v71, v10
	v_fmac_f32_e32 v11, v17, v17
	v_fma_f32 v55, v55, v2, -v4
	v_mul_f32_e32 v4, v72, v10
	v_fmac_f32_e32 v11, v114, v114
	v_fma_f32 v56, v56, v2, -v4
	v_mul_f32_e32 v4, v73, v10
	v_fmac_f32_e32 v11, v115, v115
	v_fma_f32 v57, v57, v2, -v4
	v_mul_f32_e32 v4, v74, v10
	v_fmac_f32_e32 v11, v116, v116
	v_fma_f32 v58, v58, v2, -v4
	v_mul_f32_e32 v4, v75, v10
	v_fmac_f32_e32 v11, v117, v117
	v_fma_f32 v59, v59, v2, -v4
	v_mul_f32_e32 v4, v76, v10
	v_fmac_f32_e32 v11, v118, v118
	v_fma_f32 v60, v60, v2, -v4
	v_mul_f32_e32 v4, v77, v10
	v_fmac_f32_e32 v11, v119, v119
	v_fma_f32 v61, v61, v2, -v4
	v_mul_f32_e32 v4, v78, v10
	v_fmac_f32_e32 v11, v120, v120
	v_fma_f32 v62, v62, v2, -v4
	v_mul_f32_e32 v4, v79, v10
	v_fmac_f32_e32 v11, v121, v121
	v_fma_f32 v63, v63, v2, -v4
	v_mul_f32_e32 v4, v80, v10
	v_fmac_f32_e32 v11, v122, v122
	v_fma_f32 v64, v64, v2, -v4
	v_mul_f32_e32 v4, v81, v10
	v_fmac_f32_e32 v11, v123, v123
	v_fma_f32 v65, v65, v2, -v4
	v_mul_f32_e32 v4, v34, v10
	v_fmac_f32_e32 v11, v82, v82
	v_fma_f32 v18, v18, v2, -v4
	v_mul_f32_e32 v4, v35, v10
	v_fmac_f32_e32 v11, v83, v83
	v_fma_f32 v19, v19, v2, -v4
	v_mul_f32_e32 v4, v36, v10
	v_fmac_f32_e32 v11, v84, v84
	v_fma_f32 v20, v20, v2, -v4
	v_mul_f32_e32 v4, v37, v10
	v_fmac_f32_e32 v11, v85, v85
	v_fma_f32 v21, v21, v2, -v4
	v_mul_f32_e32 v4, v38, v10
	v_fmac_f32_e32 v11, v86, v86
	v_fma_f32 v22, v22, v2, -v4
	s_waitcnt lgkmcnt(0)
	v_lshl_add_u64 v[4:5], v[196:197], 2, s[6:7]
	v_fmac_f32_e32 v11, v87, v87
	global_load_dwordx4 v[146:149], v[4:5], off
	global_load_dwordx4 v[150:153], v[4:5], off offset:32
	global_load_dwordx4 v[154:157], v[4:5], off offset:64
	global_load_dwordx4 v[158:161], v[4:5], off offset:96
	global_load_dwordx4 v[162:165], v[4:5], off offset:128
	global_load_dwordx4 v[166:169], v[4:5], off offset:160
	global_load_dwordx4 v[170:173], v[4:5], off offset:192
	global_load_dwordx4 v[174:177], v[4:5], off offset:224
	global_load_dwordx4 v[178:181], v[4:5], off offset:256
	global_load_dwordx4 v[182:185], v[4:5], off offset:288
	global_load_dwordx4 v[186:189], v[4:5], off offset:320
	global_load_dwordx4 v[190:193], v[4:5], off offset:352
	global_load_dwordx4 v[222:225], v[4:5], off offset:384
	global_load_dwordx4 v[226:229], v[4:5], off offset:416
	global_load_dwordx4 v[230:233], v[4:5], off offset:448
	global_load_dwordx4 v[234:237], v[4:5], off offset:480
	v_fmac_f32_e32 v11, v88, v88
	v_fmac_f32_e32 v11, v89, v89
	v_fmac_f32_e32 v11, v90, v90
	v_fmac_f32_e32 v11, v91, v91
	v_fmac_f32_e32 v11, v92, v92
	v_fmac_f32_e32 v11, v93, v93
	v_fmac_f32_e32 v11, v94, v94
	v_fmac_f32_e32 v11, v95, v95
	v_fmac_f32_e32 v11, v96, v96
	v_fmac_f32_e32 v11, v97, v97
	v_fmac_f32_e32 v11, v50, v50
	v_fmac_f32_e32 v11, v51, v51
	v_fmac_f32_e32 v11, v52, v52
	v_fmac_f32_e32 v11, v53, v53
	v_fmac_f32_e32 v11, v54, v54
	v_fmac_f32_e32 v11, v55, v55
	v_fmac_f32_e32 v11, v56, v56
	v_fmac_f32_e32 v11, v57, v57
	v_fmac_f32_e32 v11, v58, v58
	v_fmac_f32_e32 v11, v59, v59
	v_fmac_f32_e32 v11, v60, v60
	v_fmac_f32_e32 v11, v61, v61
	v_fmac_f32_e32 v11, v62, v62
	v_fmac_f32_e32 v11, v63, v63
	v_fmac_f32_e32 v11, v64, v64
	v_fmac_f32_e32 v11, v65, v65
	v_fmac_f32_e32 v11, v18, v18
	v_fmac_f32_e32 v11, v19, v19
	v_fmac_f32_e32 v11, v20, v20
	v_fmac_f32_e32 v11, v21, v21
	v_mul_f32_e32 v34, v39, v10
	v_fmac_f32_e32 v11, v22, v22
	v_fma_f32 v23, v23, v2, -v34
	v_mul_f32_e32 v34, v40, v10
	v_fmac_f32_e32 v11, v23, v23
	v_fma_f32 v24, v24, v2, -v34
	v_mul_f32_e32 v34, v41, v10
	v_fmac_f32_e32 v11, v24, v24
	v_fma_f32 v25, v25, v2, -v34
	v_mul_f32_e32 v34, v42, v10
	v_fmac_f32_e32 v11, v25, v25
	v_fma_f32 v26, v26, v2, -v34
	v_mul_f32_e32 v34, v43, v10
	v_fmac_f32_e32 v11, v26, v26
	v_fma_f32 v27, v27, v2, -v34
	v_mul_f32_e32 v34, v44, v10
	v_fmac_f32_e32 v11, v27, v27
	v_fma_f32 v28, v28, v2, -v34
	v_mul_f32_e32 v34, v45, v10
	v_fmac_f32_e32 v11, v28, v28
	v_fma_f32 v29, v29, v2, -v34
	v_mul_f32_e32 v34, v46, v10
	v_fmac_f32_e32 v11, v29, v29
	v_fma_f32 v30, v30, v2, -v34
	v_mul_f32_e32 v34, v47, v10
	v_fmac_f32_e32 v11, v30, v30
	v_fma_f32 v31, v31, v2, -v34
	v_mul_f32_e32 v34, v48, v10
	v_fmac_f32_e32 v11, v31, v31
	v_fma_f32 v32, v32, v2, -v34
	v_mul_f32_e32 v10, v49, v10
	v_fmac_f32_e32 v11, v32, v32
	v_fma_f32 v2, v33, v2, -v10
	v_fmac_f32_e32 v11, v2, v2
	ds_bpermute_b32 v10, v1, v11
	s_mov_b32 s6, 0xf800000
	s_add_i32 s55, s55, 1
	s_waitcnt lgkmcnt(0)
	v_add_f32_e32 v10, v11, v10
	v_mov_b32_e32 v11, 0x3727c5ac
	v_fmamk_f32 v10, v10, 0x3c000000, v11
	v_mul_f32_e32 v11, 0x4f800000, v10
	v_cmp_gt_f32_e32 vcc, s6, v10
	s_nop 1
	v_cndmask_b32_e32 v10, v10, v11, vcc
	v_sqrt_f32_e32 v11, v10
	s_nop 0
	v_add_u32_e32 v33, -1, v11
	v_fma_f32 v34, -v33, v11, v10
	v_cmp_ge_f32_e64 s[8:9], 0, v34
	v_add_u32_e32 v34, 1, v11
	s_nop 0
	v_cndmask_b32_e64 v33, v11, v33, s[8:9]
	v_fma_f32 v11, -v34, v11, v10
	v_cmp_lt_f32_e64 s[8:9], 0, v11
	s_nop 1
	v_cndmask_b32_e64 v11, v33, v34, s[8:9]
	v_mul_f32_e32 v33, 0x37800000, v11
	v_cndmask_b32_e32 v11, v11, v33, vcc
	v_mov_b32_e32 v33, 0x260
	v_cmp_class_f32_e32 vcc, v10, v33
	s_mov_b64 s[8:9], 0
	s_nop 0
	v_cndmask_b32_e32 v10, v11, v10, vcc
	v_div_scale_f32 v11, s[6:7], v10, v10, s54
	v_rcp_f32_e32 v33, v11
	s_nop 0
	v_fma_f32 v34, -v11, v33, 1.0
	v_fmac_f32_e32 v33, v34, v33
	v_div_scale_f32 v34, vcc, s54, v10, s54
	v_mul_f32_e32 v35, v34, v33
	v_fma_f32 v36, -v11, v35, v34
	v_fmac_f32_e32 v35, v36, v33
	v_fma_f32 v11, -v11, v35, v34
	v_div_fmas_f32 v11, v11, v33, v35
	v_div_fixup_f32 v33, v11, v10, s54
	v_mul_f32_e32 v12, v12, v33
	s_waitcnt vmcnt(0)
	v_mul_f32_e32 v6, v146, v12
	v_mul_f32_e32 v12, v13, v33
	v_mul_f32_e32 v7, v147, v12
	v_med3_f32 v6, v6, s48, v202
	v_med3_f32 v7, v7, s48, v202
	v_mov_b32_e32 v13, v3
	v_mul_f32_e32 v12, v14, v33
	v_cvt_pk_fp8_f32 v13, v6, v7
	v_mul_f32_e32 v8, v148, v12
	v_mul_f32_e32 v12, v15, v33
	v_mul_f32_e32 v6, v149, v12
	v_med3_f32 v7, v8, s48, v202
	v_med3_f32 v6, v6, s48, v202
	v_lshlrev_b64 v[10:11], 10, v[194:195]
	v_cvt_pk_fp8_f32 v13, v7, v6 op_sel:[0,0,1]
	v_lshl_add_u64 v[6:7], s[40:41], 0, v[10:11]
	v_lshl_add_u64 v[6:7], v[6:7], 0, s[44:45]
	v_lshl_add_u64 v[6:7], v[6:7], 0, v[196:197]
	global_store_dword v[6:7], v13, off offset:512
	v_mul_f32_e32 v12, v16, v33
	v_mov_b32_e32 v13, v3
	v_mul_f32_e32 v14, v121, v33
	v_mul_f32_e32 v15, v122, v33
	v_mul_f32_e32 v16, v123, v33
	v_mul_f32_e32 v2, v2, v33
	v_mul_f32_e32 v8, v150, v12
	v_mul_f32_e32 v12, v17, v33
	v_mul_f32_e32 v9, v151, v12
	v_med3_f32 v8, v8, s48, v202
	v_med3_f32 v9, v9, s48, v202
	v_mul_f32_e32 v12, v114, v33
	v_cvt_pk_fp8_f32 v13, v8, v9
	v_mul_f32_e32 v10, v152, v12
	v_mul_f32_e32 v12, v115, v33
	v_mul_f32_e32 v8, v153, v12
	v_med3_f32 v9, v10, s48, v202
	v_med3_f32 v8, v8, s48, v202
	v_cvt_pk_fp8_f32 v13, v9, v8 op_sel:[0,0,1]
	v_mul_f32_e32 v12, v116, v33
	global_store_dword v[6:7], v13, off offset:520
	v_mul_f32_e32 v13, v117, v33
	v_mul_f32_e32 v8, v154, v12
	v_mul_f32_e32 v9, v155, v13
	v_med3_f32 v8, v8, s48, v202
	v_med3_f32 v9, v9, s48, v202
	v_mov_b32_e32 v13, v3
	v_mul_f32_e32 v12, v118, v33
	v_cvt_pk_fp8_f32 v13, v8, v9
	v_mul_f32_e32 v10, v156, v12
	v_mul_f32_e32 v12, v119, v33
	v_mul_f32_e32 v8, v157, v12
	v_med3_f32 v9, v10, s48, v202
	v_med3_f32 v8, v8, s48, v202
	v_cvt_pk_fp8_f32 v13, v9, v8 op_sel:[0,0,1]
	v_mov_b32_e32 v12, v3
	global_store_dword v[6:7], v13, off offset:528
	v_mul_f32_e32 v13, v120, v33
	v_mul_f32_e32 v8, v158, v13
	v_mul_f32_e32 v9, v159, v14
	v_med3_f32 v8, v8, s48, v202
	v_med3_f32 v9, v9, s48, v202
	v_cvt_pk_fp8_f32 v12, v8, v9
	v_mul_f32_e32 v10, v160, v15
	v_mul_f32_e32 v8, v161, v16
	v_med3_f32 v9, v10, s48, v202
	v_med3_f32 v8, v8, s48, v202
	v_cvt_pk_fp8_f32 v12, v9, v8 op_sel:[0,0,1]
	v_mul_f32_e32 v13, v82, v33
	v_mul_f32_e32 v14, v83, v33
	v_mul_f32_e32 v15, v84, v33
	global_store_dword v[6:7], v12, off offset:536
	v_mov_b32_e32 v12, v3
	v_mul_f32_e32 v16, v85, v33
	v_mul_f32_e32 v8, v162, v13
	v_mul_f32_e32 v9, v163, v14
	v_med3_f32 v8, v8, s48, v202
	v_med3_f32 v9, v9, s48, v202
	v_cvt_pk_fp8_f32 v12, v8, v9
	v_mul_f32_e32 v10, v164, v15
	v_mul_f32_e32 v8, v165, v16
	v_med3_f32 v9, v10, s48, v202
	v_med3_f32 v8, v8, s48, v202
	v_cvt_pk_fp8_f32 v12, v9, v8 op_sel:[0,0,1]
	v_mul_f32_e32 v13, v86, v33
	v_mul_f32_e32 v14, v87, v33
	v_mul_f32_e32 v15, v88, v33
	global_store_dword v[6:7], v12, off offset:544
	v_mov_b32_e32 v12, v3
	v_mul_f32_e32 v16, v89, v33
	v_mul_f32_e32 v8, v166, v13
	v_mul_f32_e32 v9, v167, v14
	v_med3_f32 v8, v8, s48, v202
	v_med3_f32 v9, v9, s48, v202
	v_cvt_pk_fp8_f32 v12, v8, v9
	v_mul_f32_e32 v10, v168, v15
	v_mul_f32_e32 v8, v169, v16
	v_med3_f32 v9, v10, s48, v202
	v_med3_f32 v8, v8, s48, v202
	v_cvt_pk_fp8_f32 v12, v9, v8 op_sel:[0,0,1]
	v_mul_f32_e32 v13, v90, v33
	v_mul_f32_e32 v14, v91, v33
	v_mul_f32_e32 v15, v92, v33
	global_store_dword v[6:7], v12, off offset:552
	v_mov_b32_e32 v12, v3
	v_mul_f32_e32 v16, v93, v33
	v_mul_f32_e32 v8, v170, v13
	v_mul_f32_e32 v9, v171, v14
	v_med3_f32 v8, v8, s48, v202
	v_med3_f32 v9, v9, s48, v202
	v_cvt_pk_fp8_f32 v12, v8, v9
	v_mul_f32_e32 v10, v172, v15
	v_mul_f32_e32 v8, v173, v16
	v_med3_f32 v9, v10, s48, v202
	v_med3_f32 v8, v8, s48, v202
	v_cvt_pk_fp8_f32 v12, v9, v8 op_sel:[0,0,1]
	v_mul_f32_e32 v13, v94, v33
	v_mul_f32_e32 v14, v95, v33
	v_mul_f32_e32 v15, v96, v33
	global_store_dword v[6:7], v12, off offset:560
	v_mov_b32_e32 v12, v3
	v_mul_f32_e32 v16, v97, v33
	v_mul_f32_e32 v8, v174, v13
	v_mul_f32_e32 v9, v175, v14
	v_med3_f32 v8, v8, s48, v202
	v_med3_f32 v9, v9, s48, v202
	v_cvt_pk_fp8_f32 v12, v8, v9
	v_mul_f32_e32 v10, v176, v15
	v_mul_f32_e32 v8, v177, v16
	v_med3_f32 v9, v10, s48, v202
	v_med3_f32 v8, v8, s48, v202
	v_cvt_pk_fp8_f32 v12, v9, v8 op_sel:[0,0,1]
	v_mul_f32_e32 v13, v50, v33
	v_mul_f32_e32 v14, v51, v33
	v_mul_f32_e32 v15, v52, v33
	global_store_dword v[6:7], v12, off offset:568
	v_mov_b32_e32 v12, v3
	v_mul_f32_e32 v16, v53, v33
	v_mul_f32_e32 v8, v178, v13
	v_mul_f32_e32 v9, v179, v14
	v_med3_f32 v8, v8, s48, v202
	v_med3_f32 v9, v9, s48, v202
	v_cvt_pk_fp8_f32 v12, v8, v9
	v_mul_f32_e32 v10, v180, v15
	v_mul_f32_e32 v8, v181, v16
	v_med3_f32 v9, v10, s48, v202
	v_med3_f32 v8, v8, s48, v202
	v_cvt_pk_fp8_f32 v12, v9, v8 op_sel:[0,0,1]
	v_mul_f32_e32 v13, v54, v33
	v_mul_f32_e32 v14, v55, v33
	v_mul_f32_e32 v15, v56, v33
	global_store_dword v[6:7], v12, off offset:576
	v_mov_b32_e32 v12, v3
	v_mul_f32_e32 v16, v57, v33
	v_mul_f32_e32 v8, v182, v13
	v_mul_f32_e32 v9, v183, v14
	v_med3_f32 v8, v8, s48, v202
	v_med3_f32 v9, v9, s48, v202
	v_cvt_pk_fp8_f32 v12, v8, v9
	v_mul_f32_e32 v10, v184, v15
	v_mul_f32_e32 v8, v185, v16
	v_med3_f32 v9, v10, s48, v202
	v_med3_f32 v8, v8, s48, v202
	v_cvt_pk_fp8_f32 v12, v9, v8 op_sel:[0,0,1]
	v_mul_f32_e32 v13, v58, v33
	v_mul_f32_e32 v14, v59, v33
	v_mul_f32_e32 v15, v60, v33
	global_store_dword v[6:7], v12, off offset:584
	v_mov_b32_e32 v12, v3
	v_mul_f32_e32 v16, v61, v33
	v_mul_f32_e32 v8, v186, v13
	v_mul_f32_e32 v9, v187, v14
	v_med3_f32 v8, v8, s48, v202
	v_med3_f32 v9, v9, s48, v202
	v_cvt_pk_fp8_f32 v12, v8, v9
	v_mul_f32_e32 v10, v188, v15
	v_mul_f32_e32 v8, v189, v16
	v_med3_f32 v9, v10, s48, v202
	v_med3_f32 v8, v8, s48, v202
	v_cvt_pk_fp8_f32 v12, v9, v8 op_sel:[0,0,1]
	v_mul_f32_e32 v13, v62, v33
	v_mul_f32_e32 v14, v63, v33
	v_mul_f32_e32 v15, v64, v33
	global_store_dword v[6:7], v12, off offset:592
	v_mov_b32_e32 v12, v3
	v_mul_f32_e32 v16, v65, v33
	v_mul_f32_e32 v8, v190, v13
	v_mul_f32_e32 v9, v191, v14
	v_med3_f32 v8, v8, s48, v202
	v_med3_f32 v9, v9, s48, v202
	v_cvt_pk_fp8_f32 v12, v8, v9
	v_mul_f32_e32 v10, v192, v15
	v_mul_f32_e32 v8, v193, v16
	v_med3_f32 v9, v10, s48, v202
	v_med3_f32 v8, v8, s48, v202
	v_cvt_pk_fp8_f32 v12, v9, v8 op_sel:[0,0,1]
	v_mul_f32_e32 v13, v18, v33
	v_mul_f32_e32 v14, v19, v33
	v_mul_f32_e32 v15, v20, v33
	global_store_dword v[6:7], v12, off offset:600
	v_mov_b32_e32 v12, v3
	v_mul_f32_e32 v16, v21, v33
	v_mul_f32_e32 v8, v222, v13
	v_mul_f32_e32 v9, v223, v14
	v_med3_f32 v8, v8, s48, v202
	v_med3_f32 v9, v9, s48, v202
	v_cvt_pk_fp8_f32 v12, v8, v9
	v_mul_f32_e32 v10, v224, v15
	v_mul_f32_e32 v8, v225, v16
	v_med3_f32 v9, v10, s48, v202
	v_med3_f32 v8, v8, s48, v202
	v_cvt_pk_fp8_f32 v12, v9, v8 op_sel:[0,0,1]
	v_mul_f32_e32 v13, v22, v33
	v_mul_f32_e32 v14, v23, v33
	v_mul_f32_e32 v15, v24, v33
	global_store_dword v[6:7], v12, off offset:608
	v_mov_b32_e32 v12, v3
	v_mul_f32_e32 v16, v25, v33
	v_mul_f32_e32 v8, v226, v13
	v_mul_f32_e32 v9, v227, v14
	v_med3_f32 v8, v8, s48, v202
	v_med3_f32 v9, v9, s48, v202
	v_cvt_pk_fp8_f32 v12, v8, v9
	v_mul_f32_e32 v10, v228, v15
	v_mul_f32_e32 v8, v229, v16
	v_med3_f32 v9, v10, s48, v202
	v_med3_f32 v8, v8, s48, v202
	v_cvt_pk_fp8_f32 v12, v9, v8 op_sel:[0,0,1]
	v_mul_f32_e32 v13, v26, v33
	v_mul_f32_e32 v14, v27, v33
	v_mul_f32_e32 v15, v28, v33
	global_store_dword v[6:7], v12, off offset:616
	v_mov_b32_e32 v12, v3
	v_mul_f32_e32 v16, v29, v33
	v_mul_f32_e32 v8, v230, v13
	v_mul_f32_e32 v9, v231, v14
	v_med3_f32 v8, v8, s48, v202
	v_med3_f32 v9, v9, s48, v202
	v_cvt_pk_fp8_f32 v12, v8, v9
	v_mul_f32_e32 v10, v232, v15
	v_mul_f32_e32 v8, v233, v16
	v_med3_f32 v9, v10, s48, v202
	v_med3_f32 v8, v8, s48, v202
	v_cvt_pk_fp8_f32 v12, v9, v8 op_sel:[0,0,1]
	v_mul_f32_e32 v13, v32, v33
	global_store_dword v[6:7], v12, off offset:624
	v_mul_f32_e32 v5, v30, v33
	v_mul_f32_e32 v12, v31, v33
	v_mov_b32_e32 v4, v3
	v_mul_f32_e32 v5, v234, v5
	v_mul_f32_e32 v8, v235, v12
	v_med3_f32 v5, v5, s48, v202
	v_med3_f32 v8, v8, s48, v202
	v_cvt_pk_fp8_f32 v4, v5, v8
	v_mul_f32_e32 v9, v236, v13
	v_mul_f32_e32 v2, v237, v2
	v_med3_f32 v5, v9, s48, v202
	v_med3_f32 v2, v2, s48, v202
	v_cvt_pk_fp8_f32 v4, v5, v2 op_sel:[0,0,1]
	global_store_dword v[6:7], v4, off offset:632
	s_barrier

.LBB0_1297:
	v_mov_b32_e32 v8, v206
	v_mov_b32_e32 v2, v1
	s_lshl_b32 s4, s6, 8
	s_or_b32 s4, s4, s83
	v_lshl_add_u32 v2, v2, 3, s4
	s_ashr_i32 s4, s42, 11
	s_mul_hi_i32 s5, s4, 0x6000
	s_mulk_i32 s4, 0x6000
	s_add_u32 s4, s10, s4
	s_addc_u32 s5, s11, s5
	v_ashrrev_i32_e32 v3, 31, v2
	v_lshl_add_u64 v[6:7], v[2:3], 2, s[4:5]
	s_mov_b64 s[4:5], 0x405000
	v_lshl_add_u64 v[4:5], v[6:7], 0, s[4:5]
	s_add_i32 s4, s42, s77
	v_add_u32_e32 v10, s4, v8
	v_ashrrev_i32_e32 v11, 31, v10
	s_mov_b32 s4, 0x405000
	v_lshlrev_b64 v[10:11], 11, v[10:11]
	v_add_co_u32_e32 v6, vcc, s4, v6
	v_lshl_add_u64 v[10:11], s[20:21], 0, v[10:11]
	s_nop 0
	v_addc_co_u32_e32 v7, vcc, 0, v7, vcc
	v_lshl_add_u64 v[2:3], v[2:3], 1, v[10:11]
	global_load_dwordx4 v[50:53], v[4:5], off
	global_load_dwordx4 v[54:57], v[4:5], off offset:16
	global_load_dwordx4 v[58:61], v[4:5], off offset:128
	global_load_dwordx4 v[62:65], v[4:5], off offset:144
	v_mov_b32_e32 v16, v2
	v_mov_b32_e32 v17, v3
	global_load_dwordx4 v[18:21], v[16:17], off
	s_mov_b64 s[4:5], 0x8000
	v_lshl_add_u64 v[16:17], v[2:3], 0, s[4:5]
	global_load_dwordx4 v[22:25], v[16:17], off
	s_mov_b64 s[4:5], 0x10000
	v_lshl_add_u64 v[16:17], v[2:3], 0, s[4:5]
	global_load_dwordx4 v[26:29], v[16:17], off
	s_mov_b64 s[4:5], 0x18000
	v_lshl_add_u64 v[16:17], v[2:3], 0, s[4:5]
	global_load_dwordx4 v[30:33], v[16:17], off
	s_mov_b64 s[4:5], 0x40000
	v_lshl_add_u64 v[16:17], v[2:3], 0, s[4:5]
	global_load_dwordx4 v[34:37], v[16:17], off
	s_mov_b64 s[4:5], 0x48000
	v_lshl_add_u64 v[16:17], v[2:3], 0, s[4:5]
	global_load_dwordx4 v[38:41], v[16:17], off
	s_mov_b64 s[4:5], 0x50000
	v_lshl_add_u64 v[16:17], v[2:3], 0, s[4:5]
	global_load_dwordx4 v[42:45], v[16:17], off
	s_mov_b64 s[4:5], 0x58000
	v_lshl_add_u64 v[16:17], v[2:3], 0, s[4:5]
	global_load_dwordx4 v[46:49], v[16:17], off
	s_waitcnt vmcnt(8)
	v_pk_mul_f32 v[50:51], v[50:51], s[28:29] op_sel_hi:[1,0]
	v_pk_mul_f32 v[52:53], v[52:53], s[28:29] op_sel_hi:[1,0]
	v_pk_mul_f32 v[54:55], v[54:55], s[28:29] op_sel_hi:[1,0]
	v_pk_mul_f32 v[56:57], v[56:57], s[28:29] op_sel_hi:[1,0]
	v_pk_mul_f32 v[58:59], v[58:59], s[28:29] op_sel_hi:[1,0]
	v_pk_mul_f32 v[60:61], v[60:61], s[28:29] op_sel_hi:[1,0]
	v_pk_mul_f32 v[62:63], v[62:63], s[28:29] op_sel_hi:[1,0]
	v_pk_mul_f32 v[64:65], v[64:65], s[28:29] op_sel_hi:[1,0]
	s_waitcnt vmcnt(7)
	v_lshlrev_b32_e32 v8, 16, v18
	v_and_b32_e32 v9, 0xffff0000, v18
	v_lshlrev_b32_e32 v10, 16, v19
	v_and_b32_e32 v11, 0xffff0000, v19
	v_lshlrev_b32_e32 v12, 16, v20
	v_and_b32_e32 v13, 0xffff0000, v20
	v_lshlrev_b32_e32 v14, 16, v21
	v_and_b32_e32 v15, 0xffff0000, v21
	v_fmac_f32_e32 v8, v190, v50
	v_fmac_f32_e32 v9, v191, v51
	v_fmac_f32_e32 v10, v192, v52
	v_fmac_f32_e32 v11, v193, v53
	v_fmac_f32_e32 v12, v186, v54
	v_fmac_f32_e32 v13, v187, v55
	v_fmac_f32_e32 v14, v188, v56
	v_fmac_f32_e32 v15, v189, v57
	v_cvt_pk_bf16_f32 v4, v8, v9
	v_cvt_pk_bf16_f32 v5, v10, v11
	v_cvt_pk_bf16_f32 v6, v12, v13
	v_cvt_pk_bf16_f32 v7, v14, v15
	v_mov_b32_e32 v16, v2
	v_mov_b32_e32 v17, v3
	global_store_dwordx4 v[16:17], v[4:7], off
	global_load_dwordx4 v[18:21], v[16:17], off offset:64
	s_waitcnt vmcnt(8)
	v_lshlrev_b32_e32 v8, 16, v22
	v_and_b32_e32 v9, 0xffff0000, v22
	v_lshlrev_b32_e32 v10, 16, v23
	v_and_b32_e32 v11, 0xffff0000, v23
	v_lshlrev_b32_e32 v12, 16, v24
	v_and_b32_e32 v13, 0xffff0000, v24
	v_lshlrev_b32_e32 v14, 16, v25
	v_and_b32_e32 v15, 0xffff0000, v25
	v_fmac_f32_e32 v8, v182, v50
	v_fmac_f32_e32 v9, v183, v51
	v_fmac_f32_e32 v10, v184, v52
	v_fmac_f32_e32 v11, v185, v53
	v_fmac_f32_e32 v12, v178, v54
	v_fmac_f32_e32 v13, v179, v55
	v_fmac_f32_e32 v14, v180, v56
	v_fmac_f32_e32 v15, v181, v57
	v_cvt_pk_bf16_f32 v4, v8, v9
	v_cvt_pk_bf16_f32 v5, v10, v11
	v_cvt_pk_bf16_f32 v6, v12, v13
	v_cvt_pk_bf16_f32 v7, v14, v15
	s_mov_b64 s[4:5], 0x8000
	v_lshl_add_u64 v[16:17], v[2:3], 0, s[4:5]
	global_store_dwordx4 v[16:17], v[4:7], off
	global_load_dwordx4 v[22:25], v[16:17], off offset:64
	s_waitcnt vmcnt(9)
	v_lshlrev_b32_e32 v8, 16, v26
	v_and_b32_e32 v9, 0xffff0000, v26
	v_lshlrev_b32_e32 v10, 16, v27
	v_and_b32_e32 v11, 0xffff0000, v27
	v_lshlrev_b32_e32 v12, 16, v28
	v_and_b32_e32 v13, 0xffff0000, v28
	v_lshlrev_b32_e32 v14, 16, v29
	v_and_b32_e32 v15, 0xffff0000, v29
	v_fmac_f32_e32 v8, v174, v50
	v_fmac_f32_e32 v9, v175, v51
	v_fmac_f32_e32 v10, v176, v52
	v_fmac_f32_e32 v11, v177, v53
	v_fmac_f32_e32 v12, v170, v54
	v_fmac_f32_e32 v13, v171, v55
	v_fmac_f32_e32 v14, v172, v56
	v_fmac_f32_e32 v15, v173, v57
	v_cvt_pk_bf16_f32 v4, v8, v9
	v_cvt_pk_bf16_f32 v5, v10, v11
	v_cvt_pk_bf16_f32 v6, v12, v13
	v_cvt_pk_bf16_f32 v7, v14, v15
	s_mov_b64 s[4:5], 0x10000
	v_lshl_add_u64 v[16:17], v[2:3], 0, s[4:5]
	global_store_dwordx4 v[16:17], v[4:7], off
	global_load_dwordx4 v[26:29], v[16:17], off offset:64
	s_waitcnt vmcnt(10)
	v_lshlrev_b32_e32 v8, 16, v30
	v_and_b32_e32 v9, 0xffff0000, v30
	v_lshlrev_b32_e32 v10, 16, v31
	v_and_b32_e32 v11, 0xffff0000, v31
	v_lshlrev_b32_e32 v12, 16, v32
	v_and_b32_e32 v13, 0xffff0000, v32
	v_lshlrev_b32_e32 v14, 16, v33
	v_and_b32_e32 v15, 0xffff0000, v33
	v_fmac_f32_e32 v8, v166, v50
	v_fmac_f32_e32 v9, v167, v51
	v_fmac_f32_e32 v10, v168, v52
	v_fmac_f32_e32 v11, v169, v53
	v_fmac_f32_e32 v12, v162, v54
	v_fmac_f32_e32 v13, v163, v55
	v_fmac_f32_e32 v14, v164, v56
	v_fmac_f32_e32 v15, v165, v57
	v_cvt_pk_bf16_f32 v4, v8, v9
	v_cvt_pk_bf16_f32 v5, v10, v11
	v_cvt_pk_bf16_f32 v6, v12, v13
	v_cvt_pk_bf16_f32 v7, v14, v15
	s_mov_b64 s[4:5], 0x18000
	v_lshl_add_u64 v[16:17], v[2:3], 0, s[4:5]
	global_store_dwordx4 v[16:17], v[4:7], off
	global_load_dwordx4 v[30:33], v[16:17], off offset:64
	s_waitcnt vmcnt(11)
	v_lshlrev_b32_e32 v8, 16, v34
	v_and_b32_e32 v9, 0xffff0000, v34
	v_lshlrev_b32_e32 v10, 16, v35
	v_and_b32_e32 v11, 0xffff0000, v35
	v_lshlrev_b32_e32 v12, 16, v36
	v_and_b32_e32 v13, 0xffff0000, v36
	v_lshlrev_b32_e32 v14, 16, v37
	v_and_b32_e32 v15, 0xffff0000, v37
	v_fmac_f32_e32 v8, v158, v50
	v_fmac_f32_e32 v9, v159, v51
	v_fmac_f32_e32 v10, v160, v52
	v_fmac_f32_e32 v11, v161, v53
	v_fmac_f32_e32 v12, v154, v54
	v_fmac_f32_e32 v13, v155, v55
	v_fmac_f32_e32 v14, v156, v56
	v_fmac_f32_e32 v15, v157, v57
	v_cvt_pk_bf16_f32 v4, v8, v9
	v_cvt_pk_bf16_f32 v5, v10, v11
	v_cvt_pk_bf16_f32 v6, v12, v13
	v_cvt_pk_bf16_f32 v7, v14, v15
	s_mov_b64 s[4:5], 0x40000
	v_lshl_add_u64 v[16:17], v[2:3], 0, s[4:5]
	global_store_dwordx4 v[16:17], v[4:7], off
	global_load_dwordx4 v[34:37], v[16:17], off offset:64
	s_waitcnt vmcnt(12)
	v_lshlrev_b32_e32 v8, 16, v38
	v_and_b32_e32 v9, 0xffff0000, v38
	v_lshlrev_b32_e32 v10, 16, v39
	v_and_b32_e32 v11, 0xffff0000, v39
	v_lshlrev_b32_e32 v12, 16, v40
	v_and_b32_e32 v13, 0xffff0000, v40
	v_lshlrev_b32_e32 v14, 16, v41
	v_and_b32_e32 v15, 0xffff0000, v41
	v_fmac_f32_e32 v8, v150, v50
	v_fmac_f32_e32 v9, v151, v51
	v_fmac_f32_e32 v10, v152, v52
	v_fmac_f32_e32 v11, v153, v53
	v_fmac_f32_e32 v12, v146, v54
	v_fmac_f32_e32 v13, v147, v55
	v_fmac_f32_e32 v14, v148, v56
	v_fmac_f32_e32 v15, v149, v57
	v_cvt_pk_bf16_f32 v4, v8, v9
	v_cvt_pk_bf16_f32 v5, v10, v11
	v_cvt_pk_bf16_f32 v6, v12, v13
	v_cvt_pk_bf16_f32 v7, v14, v15
	s_mov_b64 s[4:5], 0x48000
	v_lshl_add_u64 v[16:17], v[2:3], 0, s[4:5]
	global_store_dwordx4 v[16:17], v[4:7], off
	global_load_dwordx4 v[38:41], v[16:17], off offset:64
	s_waitcnt vmcnt(13)
	v_lshlrev_b32_e32 v8, 16, v42
	v_and_b32_e32 v9, 0xffff0000, v42
	v_lshlrev_b32_e32 v10, 16, v43
	v_and_b32_e32 v11, 0xffff0000, v43
	v_lshlrev_b32_e32 v12, 16, v44
	v_and_b32_e32 v13, 0xffff0000, v44
	v_lshlrev_b32_e32 v14, 16, v45
	v_and_b32_e32 v15, 0xffff0000, v45
	v_fmac_f32_e32 v8, v142, v50
	v_fmac_f32_e32 v9, v143, v51
	v_fmac_f32_e32 v10, v144, v52
	v_fmac_f32_e32 v11, v145, v53
	v_fmac_f32_e32 v12, v138, v54
	v_fmac_f32_e32 v13, v139, v55
	v_fmac_f32_e32 v14, v140, v56
	v_fmac_f32_e32 v15, v141, v57
	v_cvt_pk_bf16_f32 v4, v8, v9
	v_cvt_pk_bf16_f32 v5, v10, v11
	v_cvt_pk_bf16_f32 v6, v12, v13
	v_cvt_pk_bf16_f32 v7, v14, v15
	s_mov_b64 s[4:5], 0x50000
	v_lshl_add_u64 v[16:17], v[2:3], 0, s[4:5]
	global_store_dwordx4 v[16:17], v[4:7], off
	global_load_dwordx4 v[42:45], v[16:17], off offset:64
	s_waitcnt vmcnt(14)
	v_lshlrev_b32_e32 v8, 16, v46
	v_and_b32_e32 v9, 0xffff0000, v46
	v_lshlrev_b32_e32 v10, 16, v47
	v_and_b32_e32 v11, 0xffff0000, v47
	v_lshlrev_b32_e32 v12, 16, v48
	v_and_b32_e32 v13, 0xffff0000, v48
	v_lshlrev_b32_e32 v14, 16, v49
	v_and_b32_e32 v15, 0xffff0000, v49
	v_fmac_f32_e32 v8, v134, v50
	v_fmac_f32_e32 v9, v135, v51
	v_fmac_f32_e32 v10, v136, v52
	v_fmac_f32_e32 v11, v137, v53
	v_fmac_f32_e32 v12, v130, v54
	v_fmac_f32_e32 v13, v131, v55
	v_fmac_f32_e32 v14, v132, v56
	v_fmac_f32_e32 v15, v133, v57
	v_cvt_pk_bf16_f32 v4, v8, v9
	v_cvt_pk_bf16_f32 v5, v10, v11
	v_cvt_pk_bf16_f32 v6, v12, v13
	v_cvt_pk_bf16_f32 v7, v14, v15
	s_mov_b64 s[4:5], 0x58000
	v_lshl_add_u64 v[16:17], v[2:3], 0, s[4:5]
	global_store_dwordx4 v[16:17], v[4:7], off
	global_load_dwordx4 v[46:49], v[16:17], off offset:64
	s_waitcnt vmcnt(14)
	v_lshlrev_b32_e32 v8, 16, v18
	v_and_b32_e32 v9, 0xffff0000, v18
	v_lshlrev_b32_e32 v10, 16, v19
	v_and_b32_e32 v11, 0xffff0000, v19
	v_lshlrev_b32_e32 v12, 16, v20
	v_and_b32_e32 v13, 0xffff0000, v20
	v_lshlrev_b32_e32 v14, 16, v21
	v_and_b32_e32 v15, 0xffff0000, v21
	v_fmac_f32_e32 v8, v126, v58
	v_fmac_f32_e32 v9, v127, v59
	v_fmac_f32_e32 v10, v128, v60
	v_fmac_f32_e32 v11, v129, v61
	v_fmac_f32_e32 v12, v122, v62
	v_fmac_f32_e32 v13, v123, v63
	v_fmac_f32_e32 v14, v124, v64
	v_fmac_f32_e32 v15, v125, v65
	v_cvt_pk_bf16_f32 v4, v8, v9
	v_cvt_pk_bf16_f32 v5, v10, v11
	v_cvt_pk_bf16_f32 v6, v12, v13
	v_cvt_pk_bf16_f32 v7, v14, v15
	v_mov_b32_e32 v16, v2
	v_mov_b32_e32 v17, v3
	global_store_dwordx4 v[16:17], v[4:7], off offset:64
	s_waitcnt vmcnt(13)
	v_lshlrev_b32_e32 v8, 16, v22
	v_and_b32_e32 v9, 0xffff0000, v22
	v_lshlrev_b32_e32 v10, 16, v23
	v_and_b32_e32 v11, 0xffff0000, v23
	v_lshlrev_b32_e32 v12, 16, v24
	v_and_b32_e32 v13, 0xffff0000, v24
	v_lshlrev_b32_e32 v14, 16, v25
	v_and_b32_e32 v15, 0xffff0000, v25
	v_fmac_f32_e32 v8, v118, v58
	v_fmac_f32_e32 v9, v119, v59
	v_fmac_f32_e32 v10, v120, v60
	v_fmac_f32_e32 v11, v121, v61
	v_fmac_f32_e32 v12, v114, v62
	v_fmac_f32_e32 v13, v115, v63
	v_fmac_f32_e32 v14, v116, v64
	v_fmac_f32_e32 v15, v117, v65
	v_cvt_pk_bf16_f32 v4, v8, v9
	v_cvt_pk_bf16_f32 v5, v10, v11
	v_cvt_pk_bf16_f32 v6, v12, v13
	v_cvt_pk_bf16_f32 v7, v14, v15
	s_mov_b64 s[4:5], 0x8000
	v_lshl_add_u64 v[16:17], v[2:3], 0, s[4:5]
	global_store_dwordx4 v[16:17], v[4:7], off offset:64
	s_waitcnt vmcnt(12)
	v_lshlrev_b32_e32 v8, 16, v26
	v_and_b32_e32 v9, 0xffff0000, v26
	v_lshlrev_b32_e32 v10, 16, v27
	v_and_b32_e32 v11, 0xffff0000, v27
	v_lshlrev_b32_e32 v12, 16, v28
	v_and_b32_e32 v13, 0xffff0000, v28
	v_lshlrev_b32_e32 v14, 16, v29
	v_and_b32_e32 v15, 0xffff0000, v29
	v_fmac_f32_e32 v8, v110, v58
	v_fmac_f32_e32 v9, v111, v59
	v_fmac_f32_e32 v10, v112, v60
	v_fmac_f32_e32 v11, v113, v61
	v_fmac_f32_e32 v12, v106, v62
	v_fmac_f32_e32 v13, v107, v63
	v_fmac_f32_e32 v14, v108, v64
	v_fmac_f32_e32 v15, v109, v65
	v_cvt_pk_bf16_f32 v4, v8, v9
	v_cvt_pk_bf16_f32 v5, v10, v11
	v_cvt_pk_bf16_f32 v6, v12, v13
	v_cvt_pk_bf16_f32 v7, v14, v15
	s_mov_b64 s[4:5], 0x10000
	v_lshl_add_u64 v[16:17], v[2:3], 0, s[4:5]
	global_store_dwordx4 v[16:17], v[4:7], off offset:64
	s_waitcnt vmcnt(11)
	v_lshlrev_b32_e32 v8, 16, v30
	v_and_b32_e32 v9, 0xffff0000, v30
	v_lshlrev_b32_e32 v10, 16, v31
	v_and_b32_e32 v11, 0xffff0000, v31
	v_lshlrev_b32_e32 v12, 16, v32
	v_and_b32_e32 v13, 0xffff0000, v32
	v_lshlrev_b32_e32 v14, 16, v33
	v_and_b32_e32 v15, 0xffff0000, v33
	v_fmac_f32_e32 v8, v102, v58
	v_fmac_f32_e32 v9, v103, v59
	v_fmac_f32_e32 v10, v104, v60
	v_fmac_f32_e32 v11, v105, v61
	v_fmac_f32_e32 v12, v98, v62
	v_fmac_f32_e32 v13, v99, v63
	v_fmac_f32_e32 v14, v100, v64
	v_fmac_f32_e32 v15, v101, v65
	v_cvt_pk_bf16_f32 v4, v8, v9
	v_cvt_pk_bf16_f32 v5, v10, v11
	v_cvt_pk_bf16_f32 v6, v12, v13
	v_cvt_pk_bf16_f32 v7, v14, v15
	s_mov_b64 s[4:5], 0x18000
	v_lshl_add_u64 v[16:17], v[2:3], 0, s[4:5]
	global_store_dwordx4 v[16:17], v[4:7], off offset:64
	s_waitcnt vmcnt(10)
	v_lshlrev_b32_e32 v8, 16, v34
	v_and_b32_e32 v9, 0xffff0000, v34
	v_lshlrev_b32_e32 v10, 16, v35
	v_and_b32_e32 v11, 0xffff0000, v35
	v_lshlrev_b32_e32 v12, 16, v36
	v_and_b32_e32 v13, 0xffff0000, v36
	v_lshlrev_b32_e32 v14, 16, v37
	v_and_b32_e32 v15, 0xffff0000, v37
	v_fmac_f32_e32 v8, v94, v58
	v_fmac_f32_e32 v9, v95, v59
	v_fmac_f32_e32 v10, v96, v60
	v_fmac_f32_e32 v11, v97, v61
	v_fmac_f32_e32 v12, v90, v62
	v_fmac_f32_e32 v13, v91, v63
	v_fmac_f32_e32 v14, v92, v64
	v_fmac_f32_e32 v15, v93, v65
	v_cvt_pk_bf16_f32 v4, v8, v9
	v_cvt_pk_bf16_f32 v5, v10, v11
	v_cvt_pk_bf16_f32 v6, v12, v13
	v_cvt_pk_bf16_f32 v7, v14, v15
	s_mov_b64 s[4:5], 0x40000
	v_lshl_add_u64 v[16:17], v[2:3], 0, s[4:5]
	global_store_dwordx4 v[16:17], v[4:7], off offset:64
	s_waitcnt vmcnt(9)
	v_lshlrev_b32_e32 v8, 16, v38
	v_and_b32_e32 v9, 0xffff0000, v38
	v_lshlrev_b32_e32 v10, 16, v39
	v_and_b32_e32 v11, 0xffff0000, v39
	v_lshlrev_b32_e32 v12, 16, v40
	v_and_b32_e32 v13, 0xffff0000, v40
	v_lshlrev_b32_e32 v14, 16, v41
	v_and_b32_e32 v15, 0xffff0000, v41
	v_fmac_f32_e32 v8, v86, v58
	v_fmac_f32_e32 v9, v87, v59
	v_fmac_f32_e32 v10, v88, v60
	v_fmac_f32_e32 v11, v89, v61
	v_fmac_f32_e32 v12, v82, v62
	v_fmac_f32_e32 v13, v83, v63
	v_fmac_f32_e32 v14, v84, v64
	v_fmac_f32_e32 v15, v85, v65
	v_cvt_pk_bf16_f32 v4, v8, v9
	v_cvt_pk_bf16_f32 v5, v10, v11
	v_cvt_pk_bf16_f32 v6, v12, v13
	v_cvt_pk_bf16_f32 v7, v14, v15
	s_mov_b64 s[4:5], 0x48000
	v_lshl_add_u64 v[16:17], v[2:3], 0, s[4:5]
	global_store_dwordx4 v[16:17], v[4:7], off offset:64
	s_waitcnt vmcnt(8)
	v_lshlrev_b32_e32 v8, 16, v42
	v_and_b32_e32 v9, 0xffff0000, v42
	v_lshlrev_b32_e32 v10, 16, v43
	v_and_b32_e32 v11, 0xffff0000, v43
	v_lshlrev_b32_e32 v12, 16, v44
	v_and_b32_e32 v13, 0xffff0000, v44
	v_lshlrev_b32_e32 v14, 16, v45
	v_and_b32_e32 v15, 0xffff0000, v45
	v_fmac_f32_e32 v8, v78, v58
	v_fmac_f32_e32 v9, v79, v59
	v_fmac_f32_e32 v10, v80, v60
	v_fmac_f32_e32 v11, v81, v61
	v_fmac_f32_e32 v12, v74, v62
	v_fmac_f32_e32 v13, v75, v63
	v_fmac_f32_e32 v14, v76, v64
	v_fmac_f32_e32 v15, v77, v65
	v_cvt_pk_bf16_f32 v4, v8, v9
	v_cvt_pk_bf16_f32 v5, v10, v11
	v_cvt_pk_bf16_f32 v6, v12, v13
	v_cvt_pk_bf16_f32 v7, v14, v15
	s_mov_b64 s[4:5], 0x50000
	v_lshl_add_u64 v[16:17], v[2:3], 0, s[4:5]
	global_store_dwordx4 v[16:17], v[4:7], off offset:64
	s_waitcnt vmcnt(7)
	v_lshlrev_b32_e32 v8, 16, v46
	v_and_b32_e32 v9, 0xffff0000, v46
	v_lshlrev_b32_e32 v10, 16, v47
	v_and_b32_e32 v11, 0xffff0000, v47
	v_lshlrev_b32_e32 v12, 16, v48
	v_and_b32_e32 v13, 0xffff0000, v48
	v_lshlrev_b32_e32 v14, 16, v49
	v_and_b32_e32 v15, 0xffff0000, v49
	v_fmac_f32_e32 v8, v70, v58
	v_fmac_f32_e32 v9, v71, v59
	v_fmac_f32_e32 v10, v72, v60
	v_fmac_f32_e32 v11, v73, v61
	v_fmac_f32_e32 v12, v66, v62
	v_fmac_f32_e32 v13, v67, v63
	v_fmac_f32_e32 v14, v68, v64
	v_fmac_f32_e32 v15, v69, v65
	v_cvt_pk_bf16_f32 v4, v8, v9
	v_cvt_pk_bf16_f32 v5, v10, v11
	v_cvt_pk_bf16_f32 v6, v12, v13
	v_cvt_pk_bf16_f32 v7, v14, v15
	s_mov_b64 s[4:5], 0x58000
	v_lshl_add_u64 v[16:17], v[2:3], 0, s[4:5]
	global_store_dwordx4 v[16:17], v[4:7], off offset:64
	s_and_b64 vcc, exec, s[2:3]
	s_mov_b64 s[2:3], -1
	s_cbranch_vccnz .LBB0_1273
	s_andn2_b64 vcc, exec, s[18:19]
	s_cbranch_vccnz .LBB0_1272
	s_barrier
	s_branch .LBB0_1272
